# router logits: three independent MFMA accumulator chains (hi*hi, hi*lo, lo*hi) summed at the end instead of one 48-long dependent chain; rest as previous version
# baseline (speedup 1.0000x reference)
; #define LAS __attribute__((address_space(3)))
; __global__ void __launch_bounds__(NTHR, 2) mk_fwd(Args args) {
;     ...
;                 f32x4 acc = (f32x4){0.f, 0.f, 0.f, 0.f};
; #pragma unroll
;                 for (int st = 0; st < 16; ++st) {
;                     const int kb = (kh * 512 + 32 * st + 8 * q4) * 2;
;                     const fa::bf16x8 bh = *(const LAS fa::bf16x8*)(Thi + (rh * 16 + n16) * TP + kb), bl = *(const LAS fa::bf16x8*)(Tlo + (rh * 16 + n16) * TP + kb);
;                     acc = __builtin_amdgcn_mfma_f32_16x16x32_bf16(ah[st], bh, acc, 0, 0, 0);
;                     acc = __builtin_amdgcn_mfma_f32_16x16x32_bf16(ah[st], bl, acc, 0, 0, 0);
;                     acc = __builtin_amdgcn_mfma_f32_16x16x32_bf16(*(const fa::bf16x8*)(alp + 32 * st), bh, acc, 0, 0, 0);
;                 }
;                 if (kh == 1) *(LAS f32x4*)(PART + (wave & 3) * 1024 + lane * 16) = acc;
;                 __syncthreads();
;                 if (kh == 0) { acc += *(const LAS f32x4*)(PART + (wave & 3) * 1024 + lane * 16); acc += brv; *(LAS f32x4*)(LOG + (rh * 16 + n16) * 32 + eh * 16 + 4 * q4) = acc; }
.LBB0_665:
	s_nop 0
	s_andn2_b64 vcc, exec, s[26:27]
	ds_read_b128 v[106:109], v155
	ds_read_b128 v[132:135], v156
	ds_read_b128 v[110:113], v155 offset:64
	ds_read_b128 v[136:139], v156 offset:64
	ds_read_b128 v[114:117], v155 offset:128
	ds_read_b128 v[140:143], v156 offset:128
	s_waitcnt lgkmcnt(5)
	v_mfma_f32_16x16x32_bf16 v[102:105], v[58:61], v[106:109], 0
	s_waitcnt lgkmcnt(4)
	v_mfma_f32_16x16x32_bf16 v[144:147], v[58:61], v[132:135], 0
	v_mfma_f32_16x16x32_bf16 v[160:163], v[206:209], v[106:109], 0
	ds_read_b128 v[106:109], v155 offset:192
	ds_read_b128 v[132:135], v156 offset:192
	s_waitcnt lgkmcnt(5)
	v_mfma_f32_16x16x32_bf16 v[102:105], v[2:5], v[110:113], v[102:105]
	s_waitcnt lgkmcnt(4)
	v_mfma_f32_16x16x32_bf16 v[144:147], v[2:5], v[136:139], v[144:147]
	v_mfma_f32_16x16x32_bf16 v[160:163], v[210:213], v[110:113], v[160:163]
	ds_read_b128 v[110:113], v155 offset:256
	ds_read_b128 v[136:139], v156 offset:256
	s_waitcnt lgkmcnt(5)
	v_mfma_f32_16x16x32_bf16 v[102:105], v[6:9], v[114:117], v[102:105]
	s_waitcnt lgkmcnt(4)
	v_mfma_f32_16x16x32_bf16 v[144:147], v[6:9], v[140:143], v[144:147]
	v_mfma_f32_16x16x32_bf16 v[160:163], v[214:217], v[114:117], v[160:163]
	ds_read_b128 v[114:117], v155 offset:320
	ds_read_b128 v[140:143], v156 offset:320
	s_waitcnt lgkmcnt(5)
	v_mfma_f32_16x16x32_bf16 v[102:105], v[10:13], v[106:109], v[102:105]
	s_waitcnt lgkmcnt(4)
	v_mfma_f32_16x16x32_bf16 v[144:147], v[10:13], v[132:135], v[144:147]
	v_mfma_f32_16x16x32_bf16 v[160:163], v[218:221], v[106:109], v[160:163]
	ds_read_b128 v[106:109], v155 offset:384
	ds_read_b128 v[132:135], v156 offset:384
	s_waitcnt lgkmcnt(5)
	v_mfma_f32_16x16x32_bf16 v[102:105], v[14:17], v[110:113], v[102:105]
	s_waitcnt lgkmcnt(4)
	v_mfma_f32_16x16x32_bf16 v[144:147], v[14:17], v[136:139], v[144:147]
	v_mfma_f32_16x16x32_bf16 v[160:163], v[222:225], v[110:113], v[160:163]
	ds_read_b128 v[110:113], v155 offset:448
	ds_read_b128 v[136:139], v156 offset:448
	s_waitcnt lgkmcnt(5)
	v_mfma_f32_16x16x32_bf16 v[102:105], v[18:21], v[114:117], v[102:105]
	s_waitcnt lgkmcnt(4)
	v_mfma_f32_16x16x32_bf16 v[144:147], v[18:21], v[140:143], v[144:147]
	v_mfma_f32_16x16x32_bf16 v[160:163], v[226:229], v[114:117], v[160:163]
	ds_read_b128 v[114:117], v155 offset:512
	ds_read_b128 v[140:143], v156 offset:512
	s_waitcnt lgkmcnt(5)
	v_mfma_f32_16x16x32_bf16 v[102:105], v[22:25], v[106:109], v[102:105]
	s_waitcnt lgkmcnt(4)
	v_mfma_f32_16x16x32_bf16 v[144:147], v[22:25], v[132:135], v[144:147]
	v_mfma_f32_16x16x32_bf16 v[160:163], v[230:233], v[106:109], v[160:163]
	ds_read_b128 v[106:109], v155 offset:576
	ds_read_b128 v[132:135], v156 offset:576
	s_waitcnt lgkmcnt(5)
	v_mfma_f32_16x16x32_bf16 v[102:105], v[26:29], v[110:113], v[102:105]
	s_waitcnt lgkmcnt(4)
	v_mfma_f32_16x16x32_bf16 v[144:147], v[26:29], v[136:139], v[144:147]
	v_mfma_f32_16x16x32_bf16 v[160:163], v[234:237], v[110:113], v[160:163]
	ds_read_b128 v[110:113], v155 offset:640
	ds_read_b128 v[136:139], v156 offset:640
	s_waitcnt lgkmcnt(5)
	v_mfma_f32_16x16x32_bf16 v[102:105], v[30:33], v[114:117], v[102:105]
	s_waitcnt lgkmcnt(4)
	v_mfma_f32_16x16x32_bf16 v[144:147], v[30:33], v[140:143], v[144:147]
	v_mfma_f32_16x16x32_bf16 v[160:163], v[238:241], v[114:117], v[160:163]
	ds_read_b128 v[114:117], v155 offset:704
	ds_read_b128 v[140:143], v156 offset:704
	s_waitcnt lgkmcnt(5)
	v_mfma_f32_16x16x32_bf16 v[102:105], v[34:37], v[106:109], v[102:105]
	s_waitcnt lgkmcnt(4)
	v_mfma_f32_16x16x32_bf16 v[144:147], v[34:37], v[132:135], v[144:147]
	v_mfma_f32_16x16x32_bf16 v[160:163], v[242:245], v[106:109], v[160:163]
	ds_read_b128 v[106:109], v155 offset:768
	ds_read_b128 v[132:135], v156 offset:768
	s_waitcnt lgkmcnt(5)
	v_mfma_f32_16x16x32_bf16 v[102:105], v[38:41], v[110:113], v[102:105]
	s_waitcnt lgkmcnt(4)
	v_mfma_f32_16x16x32_bf16 v[144:147], v[38:41], v[136:139], v[144:147]
	v_mfma_f32_16x16x32_bf16 v[160:163], v[246:249], v[110:113], v[160:163]
	ds_read_b128 v[110:113], v155 offset:832
	ds_read_b128 v[136:139], v156 offset:832
	s_waitcnt lgkmcnt(5)
	v_mfma_f32_16x16x32_bf16 v[102:105], v[42:45], v[114:117], v[102:105]
	s_waitcnt lgkmcnt(4)
	v_mfma_f32_16x16x32_bf16 v[144:147], v[42:45], v[140:143], v[144:147]
	v_mfma_f32_16x16x32_bf16 v[160:163], v[250:253], v[114:117], v[160:163]
	ds_read_b128 v[114:117], v155 offset:896
	ds_read_b128 v[140:143], v156 offset:896
	s_waitcnt lgkmcnt(5)
	v_mfma_f32_16x16x32_bf16 v[102:105], v[46:49], v[106:109], v[102:105]
	s_waitcnt lgkmcnt(4)
	v_mfma_f32_16x16x32_bf16 v[144:147], v[46:49], v[132:135], v[144:147]
	s_waitcnt vmcnt(11)
	v_mfma_f32_16x16x32_bf16 v[160:163], v[176:179], v[106:109], v[160:163]
	ds_read_b128 v[106:109], v155 offset:960
	ds_read_b128 v[132:135], v156 offset:960
	s_waitcnt lgkmcnt(5)
	v_mfma_f32_16x16x32_bf16 v[102:105], v[50:53], v[110:113], v[102:105]
	s_waitcnt lgkmcnt(4)
	v_mfma_f32_16x16x32_bf16 v[144:147], v[50:53], v[136:139], v[144:147]
	s_waitcnt vmcnt(10)
	v_mfma_f32_16x16x32_bf16 v[160:163], v[180:183], v[110:113], v[160:163]
	s_waitcnt lgkmcnt(3)
	v_mfma_f32_16x16x32_bf16 v[102:105], v[54:57], v[114:117], v[102:105]
	s_waitcnt lgkmcnt(2)
	v_mfma_f32_16x16x32_bf16 v[144:147], v[54:57], v[140:143], v[144:147]
	s_waitcnt vmcnt(9)
	v_mfma_f32_16x16x32_bf16 v[160:163], v[184:187], v[114:117], v[160:163]
	s_waitcnt lgkmcnt(1)
	v_mfma_f32_16x16x32_bf16 v[102:105], v[62:65], v[106:109], v[102:105]
	s_waitcnt lgkmcnt(0)
	v_mfma_f32_16x16x32_bf16 v[144:147], v[62:65], v[132:135], v[144:147]
	s_waitcnt vmcnt(8)
	v_mfma_f32_16x16x32_bf16 v[160:163], v[188:191], v[106:109], v[160:163]
	s_nop 7
	v_add_f32_e32 v144, v144, v160
	v_add_f32_e32 v145, v145, v161
	v_add_f32_e32 v146, v146, v162
	v_add_f32_e32 v147, v147, v163
	v_add_f32_e32 v102, v102, v144
	v_add_f32_e32 v103, v103, v145
	v_add_f32_e32 v104, v104, v146
	v_add_f32_e32 v105, v105, v147
	s_cbranch_vccnz .LBB0_667
	v_add_u32_e32 v106, s57, v124
	s_nop 5
	ds_write_b128 v106, v[102:105]

; #define LAS __attribute__((address_space(3)))
; __global__ void __launch_bounds__(NTHR, 2) mk_fwd(Args args) {
;     ...
;                 f32x4 acc = (f32x4){0.f, 0.f, 0.f, 0.f};
; #pragma unroll
;                 for (int st = 0; st < 16; ++st) {
;                     const int kb = (kh * 512 + 32 * st + 8 * q4) * 2;
;                     const fa::bf16x8 bh = *(const LAS fa::bf16x8*)(Thi + (rh * 16 + n16) * TP + kb), bl = *(const LAS fa::bf16x8*)(Tlo + (rh * 16 + n16) * TP + kb);
;                     acc = __builtin_amdgcn_mfma_f32_16x16x32_bf16(ah[st], bh, acc, 0, 0, 0);
;                     acc = __builtin_amdgcn_mfma_f32_16x16x32_bf16(ah[st], bl, acc, 0, 0, 0);
;                     acc = __builtin_amdgcn_mfma_f32_16x16x32_bf16(*(const fa::bf16x8*)(alp + 32 * st), bh, acc, 0, 0, 0);
;                 }
;                 if (kh == 1) *(LAS f32x4*)(PART + (wave & 3) * 1024 + lane * 16) = acc;
;                 __syncthreads();
;                 if (kh == 0) { acc += *(const LAS f32x4*)(PART + (wave & 3) * 1024 + lane * 16); acc += brv; *(LAS f32x4*)(LOG + (rh * 16 + n16) * 32 + eh * 16 + 4 * q4) = acc; }
.LBB0_1570:
	s_nop 0
	s_andn2_b64 vcc, exec, s[24:25]
	ds_read_b128 v[106:109], v155
	ds_read_b128 v[132:135], v156
	ds_read_b128 v[110:113], v155 offset:64
	ds_read_b128 v[136:139], v156 offset:64
	ds_read_b128 v[114:117], v155 offset:128
	ds_read_b128 v[140:143], v156 offset:128
	s_waitcnt lgkmcnt(5)
	v_mfma_f32_16x16x32_bf16 v[102:105], v[58:61], v[106:109], 0
	s_waitcnt lgkmcnt(4)
	v_mfma_f32_16x16x32_bf16 v[144:147], v[58:61], v[132:135], 0
	v_mfma_f32_16x16x32_bf16 v[160:163], v[206:209], v[106:109], 0
	ds_read_b128 v[106:109], v155 offset:192
	ds_read_b128 v[132:135], v156 offset:192
	s_waitcnt lgkmcnt(5)
	v_mfma_f32_16x16x32_bf16 v[102:105], v[2:5], v[110:113], v[102:105]
	s_waitcnt lgkmcnt(4)
	v_mfma_f32_16x16x32_bf16 v[144:147], v[2:5], v[136:139], v[144:147]
	v_mfma_f32_16x16x32_bf16 v[160:163], v[210:213], v[110:113], v[160:163]
	ds_read_b128 v[110:113], v155 offset:256
	ds_read_b128 v[136:139], v156 offset:256
	s_waitcnt lgkmcnt(5)
	v_mfma_f32_16x16x32_bf16 v[102:105], v[6:9], v[114:117], v[102:105]
	s_waitcnt lgkmcnt(4)
	v_mfma_f32_16x16x32_bf16 v[144:147], v[6:9], v[140:143], v[144:147]
	v_mfma_f32_16x16x32_bf16 v[160:163], v[214:217], v[114:117], v[160:163]
	ds_read_b128 v[114:117], v155 offset:320
	ds_read_b128 v[140:143], v156 offset:320
	s_waitcnt lgkmcnt(5)
	v_mfma_f32_16x16x32_bf16 v[102:105], v[10:13], v[106:109], v[102:105]
	s_waitcnt lgkmcnt(4)
	v_mfma_f32_16x16x32_bf16 v[144:147], v[10:13], v[132:135], v[144:147]
	v_mfma_f32_16x16x32_bf16 v[160:163], v[218:221], v[106:109], v[160:163]
	ds_read_b128 v[106:109], v155 offset:384
	ds_read_b128 v[132:135], v156 offset:384
	s_waitcnt lgkmcnt(5)
	v_mfma_f32_16x16x32_bf16 v[102:105], v[14:17], v[110:113], v[102:105]
	s_waitcnt lgkmcnt(4)
	v_mfma_f32_16x16x32_bf16 v[144:147], v[14:17], v[136:139], v[144:147]
	v_mfma_f32_16x16x32_bf16 v[160:163], v[222:225], v[110:113], v[160:163]
	ds_read_b128 v[110:113], v155 offset:448
	ds_read_b128 v[136:139], v156 offset:448
	s_waitcnt lgkmcnt(5)
	v_mfma_f32_16x16x32_bf16 v[102:105], v[18:21], v[114:117], v[102:105]
	s_waitcnt lgkmcnt(4)
	v_mfma_f32_16x16x32_bf16 v[144:147], v[18:21], v[140:143], v[144:147]
	v_mfma_f32_16x16x32_bf16 v[160:163], v[226:229], v[114:117], v[160:163]
	ds_read_b128 v[114:117], v155 offset:512
	ds_read_b128 v[140:143], v156 offset:512
	s_waitcnt lgkmcnt(5)
	v_mfma_f32_16x16x32_bf16 v[102:105], v[22:25], v[106:109], v[102:105]
	s_waitcnt lgkmcnt(4)
	v_mfma_f32_16x16x32_bf16 v[144:147], v[22:25], v[132:135], v[144:147]
	v_mfma_f32_16x16x32_bf16 v[160:163], v[230:233], v[106:109], v[160:163]
	ds_read_b128 v[106:109], v155 offset:576
	ds_read_b128 v[132:135], v156 offset:576
	s_waitcnt lgkmcnt(5)
	v_mfma_f32_16x16x32_bf16 v[102:105], v[26:29], v[110:113], v[102:105]
	s_waitcnt lgkmcnt(4)
	v_mfma_f32_16x16x32_bf16 v[144:147], v[26:29], v[136:139], v[144:147]
	v_mfma_f32_16x16x32_bf16 v[160:163], v[234:237], v[110:113], v[160:163]
	ds_read_b128 v[110:113], v155 offset:640
	ds_read_b128 v[136:139], v156 offset:640
	s_waitcnt lgkmcnt(5)
	v_mfma_f32_16x16x32_bf16 v[102:105], v[30:33], v[114:117], v[102:105]
	s_waitcnt lgkmcnt(4)
	v_mfma_f32_16x16x32_bf16 v[144:147], v[30:33], v[140:143], v[144:147]
	v_mfma_f32_16x16x32_bf16 v[160:163], v[238:241], v[114:117], v[160:163]
	ds_read_b128 v[114:117], v155 offset:704
	ds_read_b128 v[140:143], v156 offset:704
	s_waitcnt lgkmcnt(5)
	v_mfma_f32_16x16x32_bf16 v[102:105], v[34:37], v[106:109], v[102:105]
	s_waitcnt lgkmcnt(4)
	v_mfma_f32_16x16x32_bf16 v[144:147], v[34:37], v[132:135], v[144:147]
	v_mfma_f32_16x16x32_bf16 v[160:163], v[242:245], v[106:109], v[160:163]
	ds_read_b128 v[106:109], v155 offset:768
	ds_read_b128 v[132:135], v156 offset:768
	s_waitcnt lgkmcnt(5)
	v_mfma_f32_16x16x32_bf16 v[102:105], v[38:41], v[110:113], v[102:105]
	s_waitcnt lgkmcnt(4)
	v_mfma_f32_16x16x32_bf16 v[144:147], v[38:41], v[136:139], v[144:147]
	v_mfma_f32_16x16x32_bf16 v[160:163], v[246:249], v[110:113], v[160:163]
	ds_read_b128 v[110:113], v155 offset:832
	ds_read_b128 v[136:139], v156 offset:832
	s_waitcnt lgkmcnt(5)
	v_mfma_f32_16x16x32_bf16 v[102:105], v[42:45], v[114:117], v[102:105]
	s_waitcnt lgkmcnt(4)
	v_mfma_f32_16x16x32_bf16 v[144:147], v[42:45], v[140:143], v[144:147]
	v_mfma_f32_16x16x32_bf16 v[160:163], v[250:253], v[114:117], v[160:163]
	ds_read_b128 v[114:117], v155 offset:896
	ds_read_b128 v[140:143], v156 offset:896
	s_waitcnt lgkmcnt(5)
	v_mfma_f32_16x16x32_bf16 v[102:105], v[46:49], v[106:109], v[102:105]
	s_waitcnt lgkmcnt(4)
	v_mfma_f32_16x16x32_bf16 v[144:147], v[46:49], v[132:135], v[144:147]
	s_waitcnt vmcnt(11)
	v_mfma_f32_16x16x32_bf16 v[160:163], v[176:179], v[106:109], v[160:163]
	ds_read_b128 v[106:109], v155 offset:960
	ds_read_b128 v[132:135], v156 offset:960
	s_waitcnt lgkmcnt(5)
	v_mfma_f32_16x16x32_bf16 v[102:105], v[50:53], v[110:113], v[102:105]
	s_waitcnt lgkmcnt(4)
	v_mfma_f32_16x16x32_bf16 v[144:147], v[50:53], v[136:139], v[144:147]
	s_waitcnt vmcnt(10)
	v_mfma_f32_16x16x32_bf16 v[160:163], v[180:183], v[110:113], v[160:163]
	s_waitcnt lgkmcnt(3)
	v_mfma_f32_16x16x32_bf16 v[102:105], v[54:57], v[114:117], v[102:105]
	s_waitcnt lgkmcnt(2)
	v_mfma_f32_16x16x32_bf16 v[144:147], v[54:57], v[140:143], v[144:147]
	s_waitcnt vmcnt(9)
	v_mfma_f32_16x16x32_bf16 v[160:163], v[184:187], v[114:117], v[160:163]
	s_waitcnt lgkmcnt(1)
	v_mfma_f32_16x16x32_bf16 v[102:105], v[62:65], v[106:109], v[102:105]
	s_waitcnt lgkmcnt(0)
	v_mfma_f32_16x16x32_bf16 v[144:147], v[62:65], v[132:135], v[144:147]
	s_waitcnt vmcnt(8)
	v_mfma_f32_16x16x32_bf16 v[160:163], v[188:191], v[106:109], v[160:163]
	s_nop 7
	v_add_f32_e32 v144, v144, v160
	v_add_f32_e32 v145, v145, v161
	v_add_f32_e32 v146, v146, v162
	v_add_f32_e32 v147, v147, v163
	v_add_f32_e32 v102, v102, v144
	v_add_f32_e32 v103, v103, v145
	v_add_f32_e32 v104, v104, v146
	v_add_f32_e32 v105, v105, v147
	s_cbranch_vccnz .LBB0_1572
	v_add_u32_e32 v106, s55, v124
	s_nop 5
	ds_write_b128 v106, v[102:105]
